# v63 + three-level work-queue tail: entries 32..63 half weight-copy chunk, 64 extra copy-only quarter-chunk entries per XCD (128 entries)
# baseline (speedup 1.0000x reference)
.LBB6_896:
	s_or_b64 exec, exec, s[2:3]
	v_readlane_b32 s0, v254, 30
	s_waitcnt lgkmcnt(0)
	s_barrier
	v_mov_b32_e32 v2, s0
	ds_read_b32 v2, v2
	s_mov_b64 s[2:3], -1
	s_waitcnt lgkmcnt(0)
	s_barrier
	v_readfirstlane_b32 s0, v2
	s_cmp_gt_i32 s0, 0x7f
	s_cbranch_scc1 .LBB6_891
	s_cmp_gt_i32 s0, 47
	s_cbranch_scc0 .LBB6_899
	s_sub_i32 s1, s0, 48
	s_lshr_b32 s92, s1, 1
	s_mov_b64 s[2:3], 0

.LBB6_901:
	s_lshl_b32 s84, s0, 3
	s_or_b32 s1, s84, s59
	s_lshl_b32 s2, s1, 2
	s_lshl_b32 s3, s1, 1
	s_add_i32 s3, s3, 0x200
	s_cmp_lt_u32 s1, 0x100
	s_cselect_b32 s2, s2, s3
	s_add_i32 s3, s1, 0x400
	s_cmp_lt_u32 s1, 0x200
	s_cselect_b32 s2, s2, s3
	s_mul_i32 s2, s63, s2
	s_lshr_b32 s2, s2, 11
	s_and_b32 s90, s2, 0xffffffe0
	s_add_i32 s1, s1, 1
	s_lshl_b32 s2, s1, 2
	s_lshl_b32 s3, s1, 1
	s_add_i32 s3, s3, 0x200
	s_cmp_lt_u32 s1, 0x100
	s_cselect_b32 s2, s2, s3
	s_add_i32 s3, s1, 0x400
	s_cmp_lt_u32 s1, 0x200
	s_cselect_b32 s2, s2, s3
	s_mul_i32 s2, s63, s2
	s_lshr_b32 s2, s2, 11
	s_and_b32 s91, s2, 0xffffffe0
	s_bitcmp0_b32 s0, 0
	s_cselect_b64 s[22:23], -1, 0
	s_and_b64 vcc, exec, s[22:23]
	s_cbranch_vccnz .LBB6_1210
	v_readfirstlane_b32 s98, v0
	s_nop 0
	s_bitcmp1_b32 s98, 8
	s_cbranch_scc0 .Ldephase_a
	s_sleep 80
